# adds O5 residual epilogue batched loads; MoE epilogue biases requested right after the K-loop (before align barrier / drain / flush)
# speedup vs baseline: 1.0048x; 1.0048x over previous
.LBB0_955:
	s_lshl_b32 s2, s18, 8
	v_mov_b32_e32 v1, v0
	s_add_i32 s2, s2, s39
	s_nop 15
	s_nop 7
	s_nop 0
	v_and_or_b32 v6, v1, 15, s2
	s_lshl_b32 s2, s44, 8
	s_ashr_i32 s3, s2, 31
	s_or_b64 s[2:3], s[2:3], s[72:73]
	v_lshrrev_b32_e32 v1, 2, v1
	v_ashrrev_i32_e32 v7, 31, v6
	v_and_or_b32 v8, v1, 12, s2
	v_mov_b32_e32 v9, s3
	v_lshlrev_b64 v[4:5], 10, v[6:7]
	v_lshl_add_u64 v[4:5], v[4:5], 0, v[8:9]
	v_lshlrev_b32_e32 v230, 1, v4
	global_load_dwordx2 v[6:7], v230, s[4:5]
	global_load_dwordx2 v[8:9], v230, s[4:5] offset:32
	global_load_dwordx2 v[10:11], v230, s[4:5] offset:256
	global_load_dwordx2 v[20:21], v230, s[4:5] offset:288
	v_add_u32_e32 v231, 0x8000, v230
	global_load_dwordx2 v[22:23], v231, s[4:5]
	global_load_dwordx2 v[24:25], v231, s[4:5] offset:32
	global_load_dwordx2 v[26:27], v231, s[4:5] offset:256
	global_load_dwordx2 v[28:29], v231, s[4:5] offset:288
	v_add_u32_e32 v231, 0x10000, v230
	global_load_dwordx2 v[30:31], v231, s[4:5]
	global_load_dwordx2 v[32:33], v231, s[4:5] offset:32
	global_load_dwordx2 v[34:35], v231, s[4:5] offset:256
	global_load_dwordx2 v[36:37], v231, s[4:5] offset:288
	v_add_u32_e32 v231, 0x18000, v230
	global_load_dwordx2 v[38:39], v231, s[4:5]
	global_load_dwordx2 v[40:41], v231, s[4:5] offset:32
	global_load_dwordx2 v[42:43], v231, s[4:5] offset:256
	global_load_dwordx2 v[172:173], v231, s[4:5] offset:288
	v_add_u32_e32 v231, 0x40000, v230
	global_load_dwordx2 v[174:175], v231, s[4:5]
	global_load_dwordx2 v[176:177], v231, s[4:5] offset:32
	global_load_dwordx2 v[178:179], v231, s[4:5] offset:256
	global_load_dwordx2 v[182:183], v231, s[4:5] offset:288
	v_add_u32_e32 v231, 0x48000, v230
	global_load_dwordx2 v[184:185], v231, s[4:5]
	global_load_dwordx2 v[186:187], v231, s[4:5] offset:32
	global_load_dwordx2 v[188:189], v231, s[4:5] offset:256
	global_load_dwordx2 v[190:191], v231, s[4:5] offset:288
	v_add_u32_e32 v231, 0x50000, v230
	global_load_dwordx2 v[192:193], v231, s[4:5]
	global_load_dwordx2 v[194:195], v231, s[4:5] offset:32
	global_load_dwordx2 v[196:197], v231, s[4:5] offset:256
	global_load_dwordx2 v[204:205], v231, s[4:5] offset:288
	v_add_u32_e32 v231, 0x58000, v230
	global_load_dwordx2 v[206:207], v231, s[4:5]
	global_load_dwordx2 v[208:209], v231, s[4:5] offset:32
	global_load_dwordx2 v[210:211], v231, s[4:5] offset:256
	global_load_dwordx2 v[234:235], v231, s[4:5] offset:288
	s_waitcnt vmcnt(31)
	v_and_b32_e32 v232, 0xffff0000, v6
	v_lshlrev_b32_e32 v6, 16, v6
	v_fma_f32 v164, v164, s74, v6
	v_fma_f32 v165, v165, s74, v232
	v_and_b32_e32 v232, 0xffff0000, v7
	v_lshlrev_b32_e32 v7, 16, v7
	v_fma_f32 v166, v166, s74, v7
	v_fma_f32 v167, v167, s74, v232
	v_cvt_pk_bf16_f32 v164, v164, v165
	v_cvt_pk_bf16_f32 v165, v166, v167
	global_store_dwordx2 v230, v[164:165], s[4:5]
	s_waitcnt vmcnt(31)
	v_and_b32_e32 v232, 0xffff0000, v8
	v_lshlrev_b32_e32 v8, 16, v8
	v_fma_f32 v160, v160, s74, v8
	v_fma_f32 v161, v161, s74, v232
	v_and_b32_e32 v232, 0xffff0000, v9
	v_lshlrev_b32_e32 v9, 16, v9
	v_fma_f32 v162, v162, s74, v9
	v_fma_f32 v163, v163, s74, v232
	v_cvt_pk_bf16_f32 v160, v160, v161
	v_cvt_pk_bf16_f32 v161, v162, v163
	global_store_dwordx2 v230, v[160:161], s[4:5] offset:32
	s_waitcnt vmcnt(31)
	v_and_b32_e32 v232, 0xffff0000, v10
	v_lshlrev_b32_e32 v10, 16, v10
	v_fma_f32 v156, v156, s74, v10
	v_fma_f32 v157, v157, s74, v232
	v_and_b32_e32 v232, 0xffff0000, v11
	v_lshlrev_b32_e32 v11, 16, v11
	v_fma_f32 v158, v158, s74, v11
	v_fma_f32 v159, v159, s74, v232
	v_cvt_pk_bf16_f32 v156, v156, v157
	v_cvt_pk_bf16_f32 v157, v158, v159
	global_store_dwordx2 v230, v[156:157], s[4:5] offset:256
	s_waitcnt vmcnt(31)
	v_and_b32_e32 v232, 0xffff0000, v20
	v_lshlrev_b32_e32 v20, 16, v20
	v_fma_f32 v148, v148, s74, v20
	v_fma_f32 v149, v149, s74, v232
	v_and_b32_e32 v232, 0xffff0000, v21
	v_lshlrev_b32_e32 v21, 16, v21
	v_fma_f32 v150, v150, s74, v21
	v_fma_f32 v151, v151, s74, v232
	v_cvt_pk_bf16_f32 v148, v148, v149
	v_cvt_pk_bf16_f32 v149, v150, v151
	global_store_dwordx2 v230, v[148:149], s[4:5] offset:288
	v_add_u32_e32 v231, 0x8000, v230
	s_waitcnt vmcnt(31)
	v_and_b32_e32 v232, 0xffff0000, v22
	v_lshlrev_b32_e32 v22, 16, v22
	v_fma_f32 v152, v152, s74, v22
	v_fma_f32 v153, v153, s74, v232
	v_and_b32_e32 v232, 0xffff0000, v23
	v_lshlrev_b32_e32 v23, 16, v23
	v_fma_f32 v154, v154, s74, v23
	v_fma_f32 v155, v155, s74, v232
	v_cvt_pk_bf16_f32 v152, v152, v153
	v_cvt_pk_bf16_f32 v153, v154, v155
	global_store_dwordx2 v231, v[152:153], s[4:5]
	s_waitcnt vmcnt(31)
	v_and_b32_e32 v232, 0xffff0000, v24
	v_lshlrev_b32_e32 v24, 16, v24
	v_fma_f32 v144, v144, s74, v24
	v_fma_f32 v145, v145, s74, v232
	v_and_b32_e32 v232, 0xffff0000, v25
	v_lshlrev_b32_e32 v25, 16, v25
	v_fma_f32 v146, v146, s74, v25
	v_fma_f32 v147, v147, s74, v232
	v_cvt_pk_bf16_f32 v144, v144, v145
	v_cvt_pk_bf16_f32 v145, v146, v147
	global_store_dwordx2 v231, v[144:145], s[4:5] offset:32
	s_waitcnt vmcnt(31)
	v_and_b32_e32 v232, 0xffff0000, v26
	v_lshlrev_b32_e32 v26, 16, v26
	v_fma_f32 v140, v140, s74, v26
	v_fma_f32 v141, v141, s74, v232
	v_and_b32_e32 v232, 0xffff0000, v27
	v_lshlrev_b32_e32 v27, 16, v27
	v_fma_f32 v142, v142, s74, v27
	v_fma_f32 v143, v143, s74, v232
	v_cvt_pk_bf16_f32 v140, v140, v141
	v_cvt_pk_bf16_f32 v141, v142, v143
	global_store_dwordx2 v231, v[140:141], s[4:5] offset:256
	s_waitcnt vmcnt(31)
	v_and_b32_e32 v232, 0xffff0000, v28
	v_lshlrev_b32_e32 v28, 16, v28
	v_fma_f32 v132, v132, s74, v28
	v_fma_f32 v133, v133, s74, v232
	v_and_b32_e32 v232, 0xffff0000, v29
	v_lshlrev_b32_e32 v29, 16, v29
	v_fma_f32 v134, v134, s74, v29
	v_fma_f32 v135, v135, s74, v232
	v_cvt_pk_bf16_f32 v132, v132, v133
	v_cvt_pk_bf16_f32 v133, v134, v135
	global_store_dwordx2 v231, v[132:133], s[4:5] offset:288
	v_add_u32_e32 v231, 0x10000, v230
	s_waitcnt vmcnt(31)
	v_and_b32_e32 v232, 0xffff0000, v30
	v_lshlrev_b32_e32 v30, 16, v30
	v_fma_f32 v136, v136, s74, v30
	v_fma_f32 v137, v137, s74, v232
	v_and_b32_e32 v232, 0xffff0000, v31
	v_lshlrev_b32_e32 v31, 16, v31
	v_fma_f32 v138, v138, s74, v31
	v_fma_f32 v139, v139, s74, v232
	v_cvt_pk_bf16_f32 v136, v136, v137
	v_cvt_pk_bf16_f32 v137, v138, v139
	global_store_dwordx2 v231, v[136:137], s[4:5]
	s_waitcnt vmcnt(31)
	v_and_b32_e32 v232, 0xffff0000, v32
	v_lshlrev_b32_e32 v32, 16, v32
	v_fma_f32 v128, v128, s74, v32
	v_fma_f32 v129, v129, s74, v232
	v_and_b32_e32 v232, 0xffff0000, v33
	v_lshlrev_b32_e32 v33, 16, v33
	v_fma_f32 v130, v130, s74, v33
	v_fma_f32 v131, v131, s74, v232
	v_cvt_pk_bf16_f32 v128, v128, v129
	v_cvt_pk_bf16_f32 v129, v130, v131
	global_store_dwordx2 v231, v[128:129], s[4:5] offset:32
	s_waitcnt vmcnt(31)
	v_and_b32_e32 v232, 0xffff0000, v34
	v_lshlrev_b32_e32 v34, 16, v34
	v_fma_f32 v124, v124, s74, v34
	v_fma_f32 v125, v125, s74, v232
	v_and_b32_e32 v232, 0xffff0000, v35
	v_lshlrev_b32_e32 v35, 16, v35
	v_fma_f32 v126, v126, s74, v35
	v_fma_f32 v127, v127, s74, v232
	v_cvt_pk_bf16_f32 v124, v124, v125
	v_cvt_pk_bf16_f32 v125, v126, v127
	global_store_dwordx2 v231, v[124:125], s[4:5] offset:256
	s_waitcnt vmcnt(31)
	v_and_b32_e32 v232, 0xffff0000, v36
	v_lshlrev_b32_e32 v36, 16, v36
	v_fma_f32 v116, v116, s74, v36
	v_fma_f32 v117, v117, s74, v232
	v_and_b32_e32 v232, 0xffff0000, v37
	v_lshlrev_b32_e32 v37, 16, v37
	v_fma_f32 v118, v118, s74, v37
	v_fma_f32 v119, v119, s74, v232
	v_cvt_pk_bf16_f32 v116, v116, v117
	v_cvt_pk_bf16_f32 v117, v118, v119
	global_store_dwordx2 v231, v[116:117], s[4:5] offset:288
	v_add_u32_e32 v231, 0x18000, v230
	s_waitcnt vmcnt(31)
	v_and_b32_e32 v232, 0xffff0000, v38
	v_lshlrev_b32_e32 v38, 16, v38
	v_fma_f32 v120, v120, s74, v38
	v_fma_f32 v121, v121, s74, v232
	v_and_b32_e32 v232, 0xffff0000, v39
	v_lshlrev_b32_e32 v39, 16, v39
	v_fma_f32 v122, v122, s74, v39
	v_fma_f32 v123, v123, s74, v232
	v_cvt_pk_bf16_f32 v120, v120, v121
	v_cvt_pk_bf16_f32 v121, v122, v123
	global_store_dwordx2 v231, v[120:121], s[4:5]
	s_waitcnt vmcnt(31)
	v_and_b32_e32 v232, 0xffff0000, v40
	v_lshlrev_b32_e32 v40, 16, v40
	v_fma_f32 v112, v112, s74, v40
	v_fma_f32 v113, v113, s74, v232
	v_and_b32_e32 v232, 0xffff0000, v41
	v_lshlrev_b32_e32 v41, 16, v41
	v_fma_f32 v114, v114, s74, v41
	v_fma_f32 v115, v115, s74, v232
	v_cvt_pk_bf16_f32 v112, v112, v113
	v_cvt_pk_bf16_f32 v113, v114, v115
	global_store_dwordx2 v231, v[112:113], s[4:5] offset:32
	s_waitcnt vmcnt(31)
	v_and_b32_e32 v232, 0xffff0000, v42
	v_lshlrev_b32_e32 v42, 16, v42
	v_fma_f32 v108, v108, s74, v42
	v_fma_f32 v109, v109, s74, v232
	v_and_b32_e32 v232, 0xffff0000, v43
	v_lshlrev_b32_e32 v43, 16, v43
	v_fma_f32 v110, v110, s74, v43
	v_fma_f32 v111, v111, s74, v232
	v_cvt_pk_bf16_f32 v108, v108, v109
	v_cvt_pk_bf16_f32 v109, v110, v111
	global_store_dwordx2 v231, v[108:109], s[4:5] offset:256
	s_waitcnt vmcnt(31)
	v_and_b32_e32 v232, 0xffff0000, v172
	v_lshlrev_b32_e32 v172, 16, v172
	v_fma_f32 v104, v104, s74, v172
	v_fma_f32 v105, v105, s74, v232
	v_and_b32_e32 v232, 0xffff0000, v173
	v_lshlrev_b32_e32 v173, 16, v173
	v_fma_f32 v106, v106, s74, v173
	v_fma_f32 v107, v107, s74, v232
	v_cvt_pk_bf16_f32 v104, v104, v105
	v_cvt_pk_bf16_f32 v105, v106, v107
	global_store_dwordx2 v231, v[104:105], s[4:5] offset:288
	v_add_u32_e32 v231, 0x40000, v230
	s_waitcnt vmcnt(31)
	v_and_b32_e32 v232, 0xffff0000, v174
	v_lshlrev_b32_e32 v174, 16, v174
	v_fma_f32 v100, v100, s74, v174
	v_fma_f32 v101, v101, s74, v232
	v_and_b32_e32 v232, 0xffff0000, v175
	v_lshlrev_b32_e32 v175, 16, v175
	v_fma_f32 v102, v102, s74, v175
	v_fma_f32 v103, v103, s74, v232
	v_cvt_pk_bf16_f32 v100, v100, v101
	v_cvt_pk_bf16_f32 v101, v102, v103
	global_store_dwordx2 v231, v[100:101], s[4:5]
	s_waitcnt vmcnt(31)
	v_and_b32_e32 v232, 0xffff0000, v176
	v_lshlrev_b32_e32 v176, 16, v176
	v_fma_f32 v96, v96, s74, v176
	v_fma_f32 v97, v97, s74, v232
	v_and_b32_e32 v232, 0xffff0000, v177
	v_lshlrev_b32_e32 v177, 16, v177
	v_fma_f32 v98, v98, s74, v177
	v_fma_f32 v99, v99, s74, v232
	v_cvt_pk_bf16_f32 v96, v96, v97
	v_cvt_pk_bf16_f32 v97, v98, v99
	global_store_dwordx2 v231, v[96:97], s[4:5] offset:32
	s_waitcnt vmcnt(31)
	v_and_b32_e32 v232, 0xffff0000, v178
	v_lshlrev_b32_e32 v178, 16, v178
	v_fma_f32 v92, v92, s74, v178
	v_fma_f32 v93, v93, s74, v232
	v_and_b32_e32 v232, 0xffff0000, v179
	v_lshlrev_b32_e32 v179, 16, v179
	v_fma_f32 v94, v94, s74, v179
	v_fma_f32 v95, v95, s74, v232
	v_cvt_pk_bf16_f32 v92, v92, v93
	v_cvt_pk_bf16_f32 v93, v94, v95
	global_store_dwordx2 v231, v[92:93], s[4:5] offset:256
	s_waitcnt vmcnt(31)
	v_and_b32_e32 v232, 0xffff0000, v182
	v_lshlrev_b32_e32 v182, 16, v182
	v_fma_f32 v84, v84, s74, v182
	v_fma_f32 v85, v85, s74, v232
	v_and_b32_e32 v232, 0xffff0000, v183
	v_lshlrev_b32_e32 v183, 16, v183
	v_fma_f32 v86, v86, s74, v183
	v_fma_f32 v87, v87, s74, v232
	v_cvt_pk_bf16_f32 v84, v84, v85
	v_cvt_pk_bf16_f32 v85, v86, v87
	global_store_dwordx2 v231, v[84:85], s[4:5] offset:288
	v_add_u32_e32 v231, 0x48000, v230
	s_waitcnt vmcnt(31)
	v_and_b32_e32 v232, 0xffff0000, v184
	v_lshlrev_b32_e32 v184, 16, v184
	v_fma_f32 v88, v88, s74, v184
	v_fma_f32 v89, v89, s74, v232
	v_and_b32_e32 v232, 0xffff0000, v185
	v_lshlrev_b32_e32 v185, 16, v185
	v_fma_f32 v90, v90, s74, v185
	v_fma_f32 v91, v91, s74, v232
	v_cvt_pk_bf16_f32 v88, v88, v89
	v_cvt_pk_bf16_f32 v89, v90, v91
	global_store_dwordx2 v231, v[88:89], s[4:5]
	s_waitcnt vmcnt(31)
	v_and_b32_e32 v232, 0xffff0000, v186
	v_lshlrev_b32_e32 v186, 16, v186
	v_fma_f32 v80, v80, s74, v186
	v_fma_f32 v81, v81, s74, v232
	v_and_b32_e32 v232, 0xffff0000, v187
	v_lshlrev_b32_e32 v187, 16, v187
	v_fma_f32 v82, v82, s74, v187
	v_fma_f32 v83, v83, s74, v232
	v_cvt_pk_bf16_f32 v80, v80, v81
	v_cvt_pk_bf16_f32 v81, v82, v83
	global_store_dwordx2 v231, v[80:81], s[4:5] offset:32
	s_waitcnt vmcnt(31)
	v_and_b32_e32 v232, 0xffff0000, v188
	v_lshlrev_b32_e32 v188, 16, v188
	v_fma_f32 v76, v76, s74, v188
	v_fma_f32 v77, v77, s74, v232
	v_and_b32_e32 v232, 0xffff0000, v189
	v_lshlrev_b32_e32 v189, 16, v189
	v_fma_f32 v78, v78, s74, v189
	v_fma_f32 v79, v79, s74, v232
	v_cvt_pk_bf16_f32 v76, v76, v77
	v_cvt_pk_bf16_f32 v77, v78, v79
	global_store_dwordx2 v231, v[76:77], s[4:5] offset:256
	s_waitcnt vmcnt(31)
	v_and_b32_e32 v232, 0xffff0000, v190
	v_lshlrev_b32_e32 v190, 16, v190
	v_fma_f32 v68, v68, s74, v190
	v_fma_f32 v69, v69, s74, v232
	v_and_b32_e32 v232, 0xffff0000, v191
	v_lshlrev_b32_e32 v191, 16, v191
	v_fma_f32 v70, v70, s74, v191
	v_fma_f32 v71, v71, s74, v232
	v_cvt_pk_bf16_f32 v68, v68, v69
	v_cvt_pk_bf16_f32 v69, v70, v71
	global_store_dwordx2 v231, v[68:69], s[4:5] offset:288
	v_add_u32_e32 v231, 0x50000, v230
	s_waitcnt vmcnt(31)
	v_and_b32_e32 v232, 0xffff0000, v192
	v_lshlrev_b32_e32 v192, 16, v192
	v_fma_f32 v72, v72, s74, v192
	v_fma_f32 v73, v73, s74, v232
	v_and_b32_e32 v232, 0xffff0000, v193
	v_lshlrev_b32_e32 v193, 16, v193
	v_fma_f32 v74, v74, s74, v193
	v_fma_f32 v75, v75, s74, v232
	v_cvt_pk_bf16_f32 v72, v72, v73
	v_cvt_pk_bf16_f32 v73, v74, v75
	global_store_dwordx2 v231, v[72:73], s[4:5]
	s_waitcnt vmcnt(31)
	v_and_b32_e32 v232, 0xffff0000, v194
	v_lshlrev_b32_e32 v194, 16, v194
	v_fma_f32 v64, v64, s74, v194
	v_fma_f32 v65, v65, s74, v232
	v_and_b32_e32 v232, 0xffff0000, v195
	v_lshlrev_b32_e32 v195, 16, v195
	v_fma_f32 v66, v66, s74, v195
	v_fma_f32 v67, v67, s74, v232
	v_cvt_pk_bf16_f32 v64, v64, v65
	v_cvt_pk_bf16_f32 v65, v66, v67
	global_store_dwordx2 v231, v[64:65], s[4:5] offset:32
	s_waitcnt vmcnt(31)
	v_and_b32_e32 v232, 0xffff0000, v196
	v_lshlrev_b32_e32 v196, 16, v196
	v_fma_f32 v60, v60, s74, v196
	v_fma_f32 v61, v61, s74, v232
	v_and_b32_e32 v232, 0xffff0000, v197
	v_lshlrev_b32_e32 v197, 16, v197
	v_fma_f32 v62, v62, s74, v197
	v_fma_f32 v63, v63, s74, v232
	v_cvt_pk_bf16_f32 v60, v60, v61
	v_cvt_pk_bf16_f32 v61, v62, v63
	global_store_dwordx2 v231, v[60:61], s[4:5] offset:256
	s_waitcnt vmcnt(31)
	v_and_b32_e32 v232, 0xffff0000, v204
	v_lshlrev_b32_e32 v204, 16, v204
	v_fma_f32 v52, v52, s74, v204
	v_fma_f32 v53, v53, s74, v232
	v_and_b32_e32 v232, 0xffff0000, v205
	v_lshlrev_b32_e32 v205, 16, v205
	v_fma_f32 v54, v54, s74, v205
	v_fma_f32 v55, v55, s74, v232
	v_cvt_pk_bf16_f32 v52, v52, v53
	v_cvt_pk_bf16_f32 v53, v54, v55
	global_store_dwordx2 v231, v[52:53], s[4:5] offset:288
	v_add_u32_e32 v231, 0x58000, v230
	s_waitcnt vmcnt(31)
	v_and_b32_e32 v232, 0xffff0000, v206
	v_lshlrev_b32_e32 v206, 16, v206
	v_fma_f32 v56, v56, s74, v206
	v_fma_f32 v57, v57, s74, v232
	v_and_b32_e32 v232, 0xffff0000, v207
	v_lshlrev_b32_e32 v207, 16, v207
	v_fma_f32 v58, v58, s74, v207
	v_fma_f32 v59, v59, s74, v232
	v_cvt_pk_bf16_f32 v56, v56, v57
	v_cvt_pk_bf16_f32 v57, v58, v59
	global_store_dwordx2 v231, v[56:57], s[4:5]
	s_waitcnt vmcnt(31)
	v_and_b32_e32 v232, 0xffff0000, v208
	v_lshlrev_b32_e32 v208, 16, v208
	v_fma_f32 v48, v48, s74, v208
	v_fma_f32 v49, v49, s74, v232
	v_and_b32_e32 v232, 0xffff0000, v209
	v_lshlrev_b32_e32 v209, 16, v209
	v_fma_f32 v50, v50, s74, v209
	v_fma_f32 v51, v51, s74, v232
	v_cvt_pk_bf16_f32 v48, v48, v49
	v_cvt_pk_bf16_f32 v49, v50, v51
	global_store_dwordx2 v231, v[48:49], s[4:5] offset:32
	s_waitcnt vmcnt(31)
	v_and_b32_e32 v232, 0xffff0000, v210
	v_lshlrev_b32_e32 v210, 16, v210
	v_fma_f32 v44, v44, s74, v210
	v_fma_f32 v45, v45, s74, v232
	v_and_b32_e32 v232, 0xffff0000, v211
	v_lshlrev_b32_e32 v211, 16, v211
	v_fma_f32 v46, v46, s74, v211
	v_fma_f32 v47, v47, s74, v232
	v_cvt_pk_bf16_f32 v44, v44, v45
	v_cvt_pk_bf16_f32 v45, v46, v47
	global_store_dwordx2 v231, v[44:45], s[4:5] offset:256
	s_waitcnt vmcnt(31)
	v_and_b32_e32 v232, 0xffff0000, v234
	v_lshlrev_b32_e32 v234, 16, v234
	v_fma_f32 v12, v12, s74, v234
	v_fma_f32 v13, v13, s74, v232
	v_and_b32_e32 v232, 0xffff0000, v235
	v_lshlrev_b32_e32 v235, 16, v235
	v_fma_f32 v14, v14, s74, v235
	v_fma_f32 v15, v15, s74, v232
	v_cvt_pk_bf16_f32 v12, v12, v13
	v_cvt_pk_bf16_f32 v13, v14, v15
	global_store_dwordx2 v231, v[12:13], s[4:5] offset:288
	s_andn2_b64 vcc, exec, s[6:7]
	s_mov_b64 s[6:7], -1
	s_cbranch_vccnz .LBB0_944
	s_andn2_b64 vcc, exec, s[0:1]
	s_cbranch_vccnz .LBB0_943
	s_barrier
	s_branch .LBB0_943

.LBB0_1937:
	v_lshrrev_b32_e32 v47, 1, v0
	v_and_b32_e32 v47, 24, v47
	v_lshlrev_b32_e32 v47, 2, v47
	s_lshl_b32 s0, s7, 8
	s_ashr_i32 s1, s0, 31
	s_lshl_b64 s[0:1], s[0:1], 2
	s_cmp_lg_u32 s55, 0
	s_cbranch_scc1 .Lmoe_pf_down
	s_ashr_i32 s2, s10, 3
	s_ashr_i32 s3, s2, 31
	s_lshl_b64 s[2:3], s[2:3], 13
	s_add_u32 s2, s75, s2
	s_addc_u32 s3, s78, s3
	s_add_u32 s0, s2, s0
	s_addc_u32 s1, s3, s1
	s_lshl_b32 s2, s24, 2
	s_add_u32 s0, s0, s2
	s_addc_u32 s1, s1, 0
	s_branch .Lmoe_pf_go
.Lmoe_pf_down:
	s_ashr_i32 s2, s10, 2
	s_ashr_i32 s3, s2, 31
	s_lshl_b64 s[2:3], s[2:3], 12
	s_add_u32 s2, s79, s2
	s_addc_u32 s3, s80, s3
	s_add_u32 s0, s2, s0
	s_addc_u32 s1, s3, s1
	s_lshl_b32 s2, s24, 2
	s_add_u32 s0, s0, s2
	s_addc_u32 s1, s1, 0
.Lmoe_pf_go:
	global_load_dwordx4 v[48:51], v47, s[0:1] offset:16
	global_load_dwordx4 v[52:55], v47, s[0:1]
	global_load_dwordx4 v[56:59], v47, s[0:1] offset:528
	global_load_dwordx4 v[60:63], v47, s[0:1] offset:512
	s_and_b64 vcc, exec, s[26:27]
	s_cbranch_vccz .LBB0_1939
	s_barrier

.LBB0_1943:
	v_mov_b32_e32 v4, v0
	s_lshl_b32 s0, s7, 8
	v_and_b32_e32 v5, 15, v4
	v_lshrrev_b32_e32 v4, 1, v4
	s_lshl_b32 s2, s8, 8
	s_ashr_i32 s1, s0, 31
	v_and_b32_e32 v28, 24, v4
	v_or_b32_e32 v4, s81, v5
	s_cmp_lg_u32 s55, 0
	v_mov_b32_e32 v29, v3
	v_lshlrev_b32_e32 v46, 2, v28
	v_add_u32_e32 v30, s2, v4
	s_cbranch_scc0 .LBB0_1949
	s_ashr_i32 s2, s10, 2
	s_ashr_i32 s3, s2, 31
	s_lshl_b64 s[2:3], s[2:3], 12
	s_add_u32 s31, s79, s2
	s_addc_u32 s33, s80, s3
	s_lshl_b64 s[2:3], s[0:1], 2
	s_add_u32 s2, s31, s2
	s_addc_u32 s3, s33, s3
	s_lshl_b32 s31, s24, 2
	s_add_u32 s2, s2, s31
	s_addc_u32 s3, s3, 0
	s_mov_b32 s44, 0x3e800000
	s_mov_b32 s46, 0x41800000
	v_mov_b32_e32 v42, v3
	v_mov_b32_e32 v43, v3
	v_ashrrev_i32_e32 v31, 31, v30
	v_lshlrev_b64 v[32:33], 10, v[30:31]
	v_lshl_add_u64 v[32:33], s[22:23], 0, v[32:33]
	v_lshl_add_u64 v[32:33], v[32:33], 0, s[0:1]
	v_lshl_add_u64 v[32:33], v[32:33], 0, s[24:25]
	v_lshl_add_u64 v[32:33], v[32:33], 0, v[28:29]
	v_mov_b32_e32 v44, v3
	v_mov_b32_e32 v45, v3
	s_mov_b64 s[2:3], 0x20000
	s_waitcnt vmcnt(0)
	v_mov_b64_e32 v[20:21], v[48:49]
	v_mov_b64_e32 v[22:23], v[50:51]
	v_mov_b64_e32 v[24:25], v[52:53]
	v_mov_b64_e32 v[26:27], v[54:55]
	v_mov_b64_e32 v[4:5], v[56:57]
	v_mov_b64_e32 v[6:7], v[58:59]
	v_mov_b64_e32 v[8:9], v[60:61]
	v_mov_b64_e32 v[10:11], v[62:63]
	v_pk_mul_f32 v[20:21], v[20:21], s[46:47] op_sel_hi:[1,0]
	v_pk_mul_f32 v[22:23], v[22:23], s[46:47] op_sel_hi:[1,0]
	v_pk_mul_f32 v[24:25], v[24:25], s[46:47] op_sel_hi:[1,0]
	v_pk_mul_f32 v[26:27], v[26:27], s[46:47] op_sel_hi:[1,0]
	v_pk_mul_f32 v[4:5], v[4:5], s[46:47] op_sel_hi:[1,0]
	v_pk_mul_f32 v[6:7], v[6:7], s[46:47] op_sel_hi:[1,0]
	v_pk_mul_f32 v[8:9], v[8:9], s[46:47] op_sel_hi:[1,0]
	v_pk_mul_f32 v[10:11], v[10:11], s[46:47] op_sel_hi:[1,0]
	v_pk_fma_f32 v[40:41], v[192:193], s[44:45], v[20:21] op_sel_hi:[1,0,1]
	v_pk_fma_f32 v[36:37], v[196:197], s[44:45], v[24:25] op_sel_hi:[1,0,1]
	v_cvt_pk_fp8_f32 v43, v40, v41
	v_cvt_pk_fp8_f32 v42, v36, v37
	v_pk_fma_f32 v[34:35], v[198:199], s[44:45], v[26:27] op_sel_hi:[1,0,1]
	v_pk_fma_f32 v[38:39], v[194:195], s[44:45], v[22:23] op_sel_hi:[1,0,1]
	v_cvt_pk_fp8_f32 v42, v34, v35 op_sel:[0,0,1]
	v_cvt_pk_fp8_f32 v43, v38, v39 op_sel:[0,0,1]
	v_pk_fma_f32 v[36:37], v[164:165], s[44:45], v[8:9] op_sel_hi:[1,0,1]
	v_pk_fma_f32 v[40:41], v[160:161], s[44:45], v[4:5] op_sel_hi:[1,0,1]
	global_store_dwordx2 v[32:33], v[42:43], off
	v_mov_b32_e32 v42, v3
	v_mov_b32_e32 v43, v3
	v_cvt_pk_fp8_f32 v42, v36, v37
	v_cvt_pk_fp8_f32 v43, v40, v41
	v_pk_fma_f32 v[34:35], v[166:167], s[44:45], v[10:11] op_sel_hi:[1,0,1]
	v_pk_fma_f32 v[38:39], v[162:163], s[44:45], v[6:7] op_sel_hi:[1,0,1]
	v_cvt_pk_fp8_f32 v42, v34, v35 op_sel:[0,0,1]
	v_cvt_pk_fp8_f32 v43, v38, v39 op_sel:[0,0,1]
	v_pk_fma_f32 v[38:39], v[188:189], s[44:45], v[24:25] op_sel_hi:[1,0,1]
	v_or_b32_e32 v34, 16, v30
	global_store_dwordx2 v[32:33], v[42:43], off offset:128
	v_pk_fma_f32 v[42:43], v[184:185], s[44:45], v[20:21] op_sel_hi:[1,0,1]
	v_cvt_pk_fp8_f32 v44, v38, v39
	v_ashrrev_i32_e32 v35, 31, v34
	v_cvt_pk_fp8_f32 v45, v42, v43
	v_pk_fma_f32 v[36:37], v[190:191], s[44:45], v[26:27] op_sel_hi:[1,0,1]
	v_pk_fma_f32 v[40:41], v[186:187], s[44:45], v[22:23] op_sel_hi:[1,0,1]
	v_lshlrev_b64 v[34:35], 10, v[34:35]
	v_lshl_add_u64 v[34:35], s[22:23], 0, v[34:35]
	v_cvt_pk_fp8_f32 v44, v36, v37 op_sel:[0,0,1]
	v_cvt_pk_fp8_f32 v45, v40, v41 op_sel:[0,0,1]
	v_lshl_add_u64 v[34:35], v[34:35], 0, s[0:1]
	v_lshl_add_u64 v[34:35], v[34:35], 0, s[24:25]
	v_lshl_add_u64 v[34:35], v[34:35], 0, v[28:29]
	v_pk_fma_f32 v[38:39], v[156:157], s[44:45], v[8:9] op_sel_hi:[1,0,1]
	v_pk_fma_f32 v[42:43], v[152:153], s[44:45], v[4:5] op_sel_hi:[1,0,1]
	global_store_dwordx2 v[34:35], v[44:45], off
	v_mov_b32_e32 v44, v3
	v_mov_b32_e32 v45, v3
	v_cvt_pk_fp8_f32 v44, v38, v39
	v_cvt_pk_fp8_f32 v45, v42, v43
	v_pk_fma_f32 v[36:37], v[158:159], s[44:45], v[10:11] op_sel_hi:[1,0,1]
	v_pk_fma_f32 v[40:41], v[154:155], s[44:45], v[6:7] op_sel_hi:[1,0,1]
	v_cvt_pk_fp8_f32 v44, v36, v37 op_sel:[0,0,1]
	v_cvt_pk_fp8_f32 v45, v40, v41 op_sel:[0,0,1]
	v_pk_fma_f32 v[38:39], v[180:181], s[44:45], v[24:25] op_sel_hi:[1,0,1]
	v_pk_fma_f32 v[36:37], v[182:183], s[44:45], v[26:27] op_sel_hi:[1,0,1]
	v_mov_b64_e32 v[42:43], v[38:39]
	v_pk_fma_f32 v[38:39], v[176:177], s[44:45], v[20:21] op_sel_hi:[1,0,1]
	global_store_dwordx2 v[34:35], v[44:45], off offset:128
	v_mov_b32_e32 v44, v3
	v_mov_b32_e32 v45, v3
	v_cvt_pk_fp8_f32 v44, v42, v43
	v_cvt_pk_fp8_f32 v45, v38, v39
	v_or_b32_e32 v34, 32, v30
	v_ashrrev_i32_e32 v35, 31, v34
	v_mov_b64_e32 v[40:41], v[36:37]
	v_pk_fma_f32 v[36:37], v[178:179], s[44:45], v[22:23] op_sel_hi:[1,0,1]
	v_lshlrev_b64 v[34:35], 10, v[34:35]
	v_lshl_add_u64 v[34:35], s[22:23], 0, v[34:35]
	v_cvt_pk_fp8_f32 v44, v40, v41 op_sel:[0,0,1]
	v_cvt_pk_fp8_f32 v45, v36, v37 op_sel:[0,0,1]
	v_lshl_add_u64 v[34:35], v[34:35], 0, s[0:1]
	v_lshl_add_u64 v[34:35], v[34:35], 0, s[24:25]
	v_lshl_add_u64 v[34:35], v[34:35], 0, v[28:29]
	v_pk_fma_f32 v[38:39], v[148:149], s[44:45], v[8:9] op_sel_hi:[1,0,1]
	v_pk_fma_f32 v[42:43], v[144:145], s[44:45], v[4:5] op_sel_hi:[1,0,1]
	global_store_dwordx2 v[34:35], v[44:45], off
	v_mov_b32_e32 v44, v3
	v_mov_b32_e32 v45, v3
	v_cvt_pk_fp8_f32 v44, v38, v39
	v_cvt_pk_fp8_f32 v45, v42, v43
	v_pk_fma_f32 v[36:37], v[150:151], s[44:45], v[10:11] op_sel_hi:[1,0,1]
	v_pk_fma_f32 v[40:41], v[146:147], s[44:45], v[6:7] op_sel_hi:[1,0,1]
	v_cvt_pk_fp8_f32 v44, v36, v37 op_sel:[0,0,1]
	v_cvt_pk_fp8_f32 v45, v40, v41 op_sel:[0,0,1]
	v_pk_fma_f32 v[38:39], v[172:173], s[44:45], v[24:25] op_sel_hi:[1,0,1]
	v_pk_fma_f32 v[42:43], v[168:169], s[44:45], v[20:21] op_sel_hi:[1,0,1]
	global_store_dwordx2 v[34:35], v[44:45], off offset:128
	v_mov_b32_e32 v44, v3
	v_mov_b32_e32 v45, v3
	v_cvt_pk_fp8_f32 v44, v38, v39
	v_cvt_pk_fp8_f32 v45, v42, v43
	v_or_b32_e32 v34, 48, v30
	v_ashrrev_i32_e32 v35, 31, v34
	v_pk_fma_f32 v[36:37], v[174:175], s[44:45], v[26:27] op_sel_hi:[1,0,1]
	v_pk_fma_f32 v[40:41], v[170:171], s[44:45], v[22:23] op_sel_hi:[1,0,1]
	v_lshlrev_b64 v[34:35], 10, v[34:35]
	v_lshl_add_u64 v[34:35], s[22:23], 0, v[34:35]
	v_cvt_pk_fp8_f32 v44, v36, v37 op_sel:[0,0,1]
	v_cvt_pk_fp8_f32 v45, v40, v41 op_sel:[0,0,1]
	v_lshl_add_u64 v[34:35], v[34:35], 0, s[0:1]
	v_lshl_add_u64 v[34:35], v[34:35], 0, s[24:25]
	v_lshl_add_u64 v[34:35], v[34:35], 0, v[28:29]
	v_pk_fma_f32 v[38:39], v[140:141], s[44:45], v[8:9] op_sel_hi:[1,0,1]
	v_pk_fma_f32 v[42:43], v[136:137], s[44:45], v[4:5] op_sel_hi:[1,0,1]
	global_store_dwordx2 v[34:35], v[44:45], off
	v_mov_b32_e32 v44, v3
	v_mov_b32_e32 v45, v3
	v_cvt_pk_fp8_f32 v44, v38, v39
	v_cvt_pk_fp8_f32 v45, v42, v43
	v_pk_fma_f32 v[36:37], v[142:143], s[44:45], v[10:11] op_sel_hi:[1,0,1]
	v_pk_fma_f32 v[40:41], v[138:139], s[44:45], v[6:7] op_sel_hi:[1,0,1]
	v_cvt_pk_fp8_f32 v44, v36, v37 op_sel:[0,0,1]
	v_cvt_pk_fp8_f32 v45, v40, v41 op_sel:[0,0,1]
	v_pk_fma_f32 v[38:39], v[132:133], s[44:45], v[24:25] op_sel_hi:[1,0,1]
	v_pk_fma_f32 v[42:43], v[128:129], s[44:45], v[20:21] op_sel_hi:[1,0,1]
	global_store_dwordx2 v[34:35], v[44:45], off offset:128
	v_mov_b32_e32 v44, v3
	v_mov_b32_e32 v45, v3
	v_cvt_pk_fp8_f32 v44, v38, v39
	v_cvt_pk_fp8_f32 v45, v42, v43
	v_pk_fma_f32 v[36:37], v[134:135], s[44:45], v[26:27] op_sel_hi:[1,0,1]
	v_pk_fma_f32 v[40:41], v[130:131], s[44:45], v[22:23] op_sel_hi:[1,0,1]
	v_cvt_pk_fp8_f32 v44, v36, v37 op_sel:[0,0,1]
	v_cvt_pk_fp8_f32 v45, v40, v41 op_sel:[0,0,1]
	v_lshl_add_u64 v[34:35], v[32:33], 0, s[2:3]
	s_mov_b32 s2, 0x20000
	v_add_co_u32_e32 v36, vcc, s2, v32
	v_pk_fma_f32 v[38:39], v[100:101], s[44:45], v[8:9] op_sel_hi:[1,0,1]
	s_nop 0
	v_addc_co_u32_e32 v37, vcc, 0, v33, vcc
	v_pk_fma_f32 v[42:43], v[96:97], s[44:45], v[4:5] op_sel_hi:[1,0,1]
	global_store_dwordx2 v[36:37], v[44:45], off
	v_mov_b32_e32 v44, v3
	v_mov_b32_e32 v45, v3
	v_cvt_pk_fp8_f32 v44, v38, v39
	v_cvt_pk_fp8_f32 v45, v42, v43
	v_pk_fma_f32 v[36:37], v[102:103], s[44:45], v[10:11] op_sel_hi:[1,0,1]
	v_pk_fma_f32 v[40:41], v[98:99], s[44:45], v[6:7] op_sel_hi:[1,0,1]
	v_cvt_pk_fp8_f32 v44, v36, v37 op_sel:[0,0,1]
	v_cvt_pk_fp8_f32 v45, v40, v41 op_sel:[0,0,1]
	v_pk_fma_f32 v[38:39], v[124:125], s[44:45], v[24:25] op_sel_hi:[1,0,1]
	v_pk_fma_f32 v[42:43], v[120:121], s[44:45], v[20:21] op_sel_hi:[1,0,1]
	global_store_dwordx2 v[34:35], v[44:45], off offset:128
	v_mov_b32_e32 v44, v3
	v_mov_b32_e32 v45, v3
	v_cvt_pk_fp8_f32 v44, v38, v39
	v_cvt_pk_fp8_f32 v45, v42, v43
	v_pk_fma_f32 v[36:37], v[126:127], s[44:45], v[26:27] op_sel_hi:[1,0,1]
	v_pk_fma_f32 v[40:41], v[122:123], s[44:45], v[22:23] op_sel_hi:[1,0,1]
	s_mov_b64 s[2:3], 0x24000
	v_cvt_pk_fp8_f32 v44, v36, v37 op_sel:[0,0,1]
	v_cvt_pk_fp8_f32 v45, v40, v41 op_sel:[0,0,1]
	v_lshl_add_u64 v[34:35], v[32:33], 0, s[2:3]
	s_mov_b32 s2, 0x24000
	v_add_co_u32_e32 v36, vcc, s2, v32
	v_pk_fma_f32 v[38:39], v[92:93], s[44:45], v[8:9] op_sel_hi:[1,0,1]
	s_nop 0
	v_addc_co_u32_e32 v37, vcc, 0, v33, vcc
	v_pk_fma_f32 v[42:43], v[88:89], s[44:45], v[4:5] op_sel_hi:[1,0,1]
	global_store_dwordx2 v[36:37], v[44:45], off
	v_mov_b32_e32 v44, v3
	v_mov_b32_e32 v45, v3
	v_cvt_pk_fp8_f32 v44, v38, v39
	v_cvt_pk_fp8_f32 v45, v42, v43
	v_pk_fma_f32 v[36:37], v[94:95], s[44:45], v[10:11] op_sel_hi:[1,0,1]
	v_pk_fma_f32 v[40:41], v[90:91], s[44:45], v[6:7] op_sel_hi:[1,0,1]
	v_cvt_pk_fp8_f32 v44, v36, v37 op_sel:[0,0,1]
	v_cvt_pk_fp8_f32 v45, v40, v41 op_sel:[0,0,1]
	v_pk_fma_f32 v[38:39], v[116:117], s[44:45], v[24:25] op_sel_hi:[1,0,1]
	v_pk_fma_f32 v[42:43], v[112:113], s[44:45], v[20:21] op_sel_hi:[1,0,1]
	global_store_dwordx2 v[34:35], v[44:45], off offset:128
	v_mov_b32_e32 v44, v3
	v_mov_b32_e32 v45, v3
	v_cvt_pk_fp8_f32 v44, v38, v39
	v_cvt_pk_fp8_f32 v45, v42, v43
	v_pk_fma_f32 v[36:37], v[118:119], s[44:45], v[26:27] op_sel_hi:[1,0,1]
	v_pk_fma_f32 v[40:41], v[114:115], s[44:45], v[22:23] op_sel_hi:[1,0,1]
	s_mov_b64 s[2:3], 0x28000
	v_cvt_pk_fp8_f32 v44, v36, v37 op_sel:[0,0,1]
	v_cvt_pk_fp8_f32 v45, v40, v41 op_sel:[0,0,1]
	v_lshl_add_u64 v[34:35], v[32:33], 0, s[2:3]
	s_mov_b32 s2, 0x28000
	v_add_co_u32_e32 v36, vcc, s2, v32
	v_pk_fma_f32 v[38:39], v[84:85], s[44:45], v[8:9] op_sel_hi:[1,0,1]
	s_nop 0
	v_addc_co_u32_e32 v37, vcc, 0, v33, vcc
	global_store_dwordx2 v[36:37], v[44:45], off
	v_mov_b32_e32 v44, v3
	v_pk_fma_f32 v[42:43], v[80:81], s[44:45], v[4:5] op_sel_hi:[1,0,1]
	v_cvt_pk_fp8_f32 v44, v38, v39
	v_mov_b32_e32 v45, v3
	v_pk_fma_f32 v[36:37], v[86:87], s[44:45], v[10:11] op_sel_hi:[1,0,1]
	v_cvt_pk_fp8_f32 v45, v42, v43
	v_pk_fma_f32 v[24:25], v[108:109], s[44:45], v[24:25] op_sel_hi:[1,0,1]
	v_pk_fma_f32 v[20:21], v[104:105], s[44:45], v[20:21] op_sel_hi:[1,0,1]
	v_pk_fma_f32 v[40:41], v[82:83], s[44:45], v[6:7] op_sel_hi:[1,0,1]
	v_cvt_pk_fp8_f32 v44, v36, v37 op_sel:[0,0,1]
	v_mov_b32_e32 v36, v3
	v_mov_b32_e32 v37, v3
	v_cvt_pk_fp8_f32 v36, v24, v25
	v_cvt_pk_fp8_f32 v37, v20, v21
	v_cvt_pk_fp8_f32 v45, v40, v41 op_sel:[0,0,1]
	v_pk_fma_f32 v[26:27], v[110:111], s[44:45], v[26:27] op_sel_hi:[1,0,1]
	v_pk_fma_f32 v[22:23], v[106:107], s[44:45], v[22:23] op_sel_hi:[1,0,1]
	s_mov_b64 s[2:3], 0x2c000
	v_cvt_pk_fp8_f32 v36, v26, v27 op_sel:[0,0,1]
	v_cvt_pk_fp8_f32 v37, v22, v23 op_sel:[0,0,1]
	global_store_dwordx2 v[34:35], v[44:45], off offset:128
	v_lshl_add_u64 v[34:35], v[32:33], 0, s[2:3]
	s_mov_b32 s2, 0x2c000
	v_add_co_u32_e32 v20, vcc, s2, v32
	v_pk_fma_f32 v[8:9], v[76:77], s[44:45], v[8:9] op_sel_hi:[1,0,1]
	s_nop 0
	v_addc_co_u32_e32 v21, vcc, 0, v33, vcc
	v_pk_fma_f32 v[4:5], v[12:13], s[44:45], v[4:5] op_sel_hi:[1,0,1]
	global_store_dwordx2 v[20:21], v[36:37], off
	v_mov_b32_e32 v20, v3
	v_mov_b32_e32 v21, v3
	v_cvt_pk_fp8_f32 v20, v8, v9
	v_cvt_pk_fp8_f32 v21, v4, v5
	v_pk_fma_f32 v[10:11], v[78:79], s[44:45], v[10:11] op_sel_hi:[1,0,1]
	v_pk_fma_f32 v[6:7], v[14:15], s[44:45], v[6:7] op_sel_hi:[1,0,1]
	v_cvt_pk_fp8_f32 v20, v10, v11 op_sel:[0,0,1]
	v_cvt_pk_fp8_f32 v21, v6, v7 op_sel:[0,0,1]
	global_store_dwordx2 v[34:35], v[20:21], off offset:128
	s_cbranch_execnz .LBB0_1946
.LBB0_1945:
	s_ashr_i32 s2, s10, 3
	s_ashr_i32 s3, s2, 31
	s_lshl_b64 s[2:3], s[2:3], 13
	s_add_u32 s2, s75, s2
	s_addc_u32 s3, s78, s3
	s_lshl_b64 s[0:1], s[0:1], 2
	s_add_u32 s0, s2, s0
	s_addc_u32 s1, s3, s1
	s_lshl_b32 s2, s24, 2
	s_add_u32 s0, s0, s2
	s_addc_u32 s1, s1, 0
	v_ashrrev_i32_e32 v31, 31, v30
	s_mov_b32 s2, 0xc0c00000
	s_lshl_b32 s0, s7, 7
	s_ashr_i32 s1, s0, 31
	s_mov_b32 s72, s6
	s_waitcnt vmcnt(0)
	v_mov_b64_e32 v[4:5], v[48:49]
	v_mov_b64_e32 v[6:7], v[50:51]
	v_mov_b64_e32 v[8:9], v[52:53]
	v_mov_b64_e32 v[10:11], v[54:55]
	v_mov_b64_e32 v[22:23], v[56:57]
	v_mov_b64_e32 v[24:25], v[58:59]
	v_mov_b64_e32 v[32:33], v[60:61]
	v_mov_b64_e32 v[34:35], v[62:63]
	v_pk_add_f32 v[20:21], v[24:25], 1.0 op_sel_hi:[1,0]
	v_lshlrev_b64 v[24:25], 10, v[30:31]
	v_fmamk_f32 v31, v196, 0x3c800000, v8
	v_min_f32_e32 v31, 0x40e00000, v31
	v_pk_add_f32 v[26:27], v[34:35], 1.0 op_sel_hi:[1,0]
	v_mul_f32_e32 v35, 0xc01d265f, v31
	v_exp_f32_e32 v35, v35
	v_pk_add_f32 v[32:33], v[32:33], 1.0 op_sel_hi:[1,0]
	v_pk_add_f32 v[22:23], v[22:23], 1.0 op_sel_hi:[1,0]
	v_fmamk_f32 v34, v164, 0x3c800000, v32
	v_add_f32_e32 v35, 1.0, v35
	v_rcp_f32_e32 v35, v35
	v_med3_f32 v34, v34, s2, v250
	v_lshl_add_u64 v[24:25], s[14:15], 0, v[24:25]
	v_lshl_add_u64 v[24:25], v[24:25], 0, s[0:1]
	v_mul_f32_e32 v31, v31, v35
	v_mul_f32_e32 v31, v34, v31
	v_fmamk_f32 v34, v197, 0x3c800000, v9
	v_min_f32_e32 v34, 0x40e00000, v34
	v_mul_f32_e32 v36, 0xc01d265f, v34
	v_exp_f32_e32 v36, v36
	v_fmamk_f32 v35, v165, 0x3c800000, v33
	v_med3_f32 v35, v35, s2, v250
	v_lshl_add_u64 v[24:25], v[24:25], 0, s[24:25]
	v_add_f32_e32 v36, 1.0, v36
	v_rcp_f32_e32 v36, v36
	v_lshl_add_u64 v[24:25], v[24:25], 0, v[28:29]
	v_mul_f32_e32 v34, v34, v36
	v_mul_f32_e32 v35, v35, v34
	v_fmamk_f32 v34, v198, 0x3c800000, v10
	v_min_f32_e32 v34, 0x40e00000, v34
	v_mul_f32_e32 v37, 0xc01d265f, v34
	v_exp_f32_e32 v37, v37
	v_fmamk_f32 v36, v166, 0x3c800000, v26
	v_med3_f32 v36, v36, s2, v250
	v_add_f32_e32 v37, 1.0, v37
	v_rcp_f32_e32 v37, v37
	s_nop 0
	v_mul_f32_e32 v34, v34, v37
	v_mul_f32_e32 v36, v36, v34
	v_fmamk_f32 v34, v199, 0x3c800000, v11
	v_min_f32_e32 v34, 0x40e00000, v34
	v_mul_f32_e32 v38, 0xc01d265f, v34
	v_exp_f32_e32 v38, v38
	v_fmamk_f32 v37, v167, 0x3c800000, v27
	v_med3_f32 v37, v37, s2, v250
	v_add_f32_e32 v38, 1.0, v38
	v_rcp_f32_e32 v38, v38
	s_nop 0
	v_mul_f32_e32 v34, v34, v38
	v_mul_f32_e32 v37, v37, v34
	v_fmamk_f32 v34, v192, 0x3c800000, v4
	v_min_f32_e32 v34, 0x40e00000, v34
	v_mul_f32_e32 v39, 0xc01d265f, v34
	v_exp_f32_e32 v39, v39
	v_fmamk_f32 v38, v160, 0x3c800000, v22
	v_med3_f32 v38, v38, s2, v250
	v_add_f32_e32 v39, 1.0, v39
	v_rcp_f32_e32 v39, v39
	s_nop 0
	v_mul_f32_e32 v34, v34, v39
	v_mul_f32_e32 v38, v38, v34
	v_fmamk_f32 v34, v193, 0x3c800000, v5
	v_min_f32_e32 v34, 0x40e00000, v34
	v_mul_f32_e32 v40, 0xc01d265f, v34
	v_exp_f32_e32 v40, v40
	v_fmamk_f32 v39, v161, 0x3c800000, v23
	v_med3_f32 v39, v39, s2, v250
	v_add_f32_e32 v40, 1.0, v40
	v_rcp_f32_e32 v40, v40
	s_nop 0
	v_mul_f32_e32 v34, v34, v40
	v_mul_f32_e32 v40, v39, v34
	v_fmamk_f32 v34, v194, 0x3c800000, v6
	v_min_f32_e32 v34, 0x40e00000, v34
	v_mul_f32_e32 v41, 0xc01d265f, v34
	v_exp_f32_e32 v41, v41
	v_fmamk_f32 v39, v162, 0x3c800000, v20
	v_med3_f32 v39, v39, s2, v250
	v_add_f32_e32 v41, 1.0, v41
	v_rcp_f32_e32 v41, v41
	s_nop 0
	v_mul_f32_e32 v34, v34, v41
	v_mul_f32_e32 v39, v39, v34
	v_fmamk_f32 v34, v195, 0x3c800000, v7
	v_min_f32_e32 v34, 0x40e00000, v34
	v_mul_f32_e32 v42, 0xc01d265f, v34
	v_exp_f32_e32 v42, v42
	v_fmamk_f32 v41, v163, 0x3c800000, v21
	v_med3_f32 v41, v41, s2, v250
	v_add_f32_e32 v42, 1.0, v42
	v_rcp_f32_e32 v42, v42
	s_nop 0
	v_mul_f32_e32 v34, v34, v42
	v_mul_f32_e32 v41, v41, v34
	v_mov_b32_e32 v34, v3
	v_cvt_pk_fp8_f32 v34, v31, v35
	v_fmamk_f32 v31, v188, 0x3c800000, v8
	v_min_f32_e32 v31, 0x40e00000, v31
	v_mov_b32_e32 v35, v3
	v_cvt_pk_fp8_f32 v34, v36, v37 op_sel:[0,0,1]
	v_mul_f32_e32 v37, 0xc01d265f, v31
	v_exp_f32_e32 v37, v37
	v_fmamk_f32 v36, v156, 0x3c800000, v32
	v_med3_f32 v36, v36, s2, v250
	v_cvt_pk_fp8_f32 v35, v38, v40
	v_add_f32_e32 v37, 1.0, v37
	v_rcp_f32_e32 v37, v37
	v_cvt_pk_fp8_f32 v35, v39, v41 op_sel:[0,0,1]
	s_nop 0
	global_store_dwordx2 v[24:25], v[34:35], off sc1
	v_mul_f32_e32 v31, v31, v37
	v_mul_f32_e32 v31, v36, v31
	v_fmamk_f32 v36, v189, 0x3c800000, v9
	v_min_f32_e32 v36, 0x40e00000, v36
	v_mul_f32_e32 v38, 0xc01d265f, v36
	v_exp_f32_e32 v38, v38
	v_fmamk_f32 v37, v157, 0x3c800000, v33
	v_med3_f32 v37, v37, s2, v250
	v_or_b32_e32 v34, 16, v30
	v_add_f32_e32 v38, 1.0, v38
	v_rcp_f32_e32 v38, v38
	v_ashrrev_i32_e32 v35, 31, v34
	v_lshlrev_b64 v[34:35], 10, v[34:35]
	v_lshl_add_u64 v[34:35], s[14:15], 0, v[34:35]
	v_mul_f32_e32 v36, v36, v38
	v_mul_f32_e32 v37, v37, v36
	v_fmamk_f32 v36, v190, 0x3c800000, v10
	v_min_f32_e32 v36, 0x40e00000, v36
	v_mul_f32_e32 v39, 0xc01d265f, v36
	v_exp_f32_e32 v39, v39
	v_fmamk_f32 v38, v158, 0x3c800000, v26
	v_med3_f32 v38, v38, s2, v250
	v_lshl_add_u64 v[34:35], v[34:35], 0, s[0:1]
	v_add_f32_e32 v39, 1.0, v39
	v_rcp_f32_e32 v39, v39
	v_lshl_add_u64 v[34:35], v[34:35], 0, s[24:25]
	v_lshl_add_u64 v[34:35], v[34:35], 0, v[28:29]
	v_mul_f32_e32 v36, v36, v39
	v_mul_f32_e32 v38, v38, v36
	v_fmamk_f32 v36, v191, 0x3c800000, v11
	v_min_f32_e32 v36, 0x40e00000, v36
	v_mul_f32_e32 v40, 0xc01d265f, v36
	v_exp_f32_e32 v40, v40
	v_fmamk_f32 v39, v159, 0x3c800000, v27
	v_med3_f32 v39, v39, s2, v250
	v_add_f32_e32 v40, 1.0, v40
	v_rcp_f32_e32 v40, v40
	s_nop 0
	v_mul_f32_e32 v36, v36, v40
	v_mul_f32_e32 v39, v39, v36
	v_fmamk_f32 v36, v184, 0x3c800000, v4
	v_min_f32_e32 v36, 0x40e00000, v36
	v_mul_f32_e32 v41, 0xc01d265f, v36
	v_exp_f32_e32 v41, v41
	v_fmamk_f32 v40, v152, 0x3c800000, v22
	v_med3_f32 v40, v40, s2, v250
	v_add_f32_e32 v41, 1.0, v41
	v_rcp_f32_e32 v41, v41
	s_nop 0
	v_mul_f32_e32 v36, v36, v41
	v_mul_f32_e32 v40, v40, v36
	v_fmamk_f32 v36, v185, 0x3c800000, v5
	v_min_f32_e32 v36, 0x40e00000, v36
	v_mul_f32_e32 v42, 0xc01d265f, v36
	v_exp_f32_e32 v42, v42
	v_fmamk_f32 v41, v153, 0x3c800000, v23
	v_med3_f32 v41, v41, s2, v250
	v_add_f32_e32 v42, 1.0, v42
	v_rcp_f32_e32 v42, v42
	s_nop 0
	v_mul_f32_e32 v36, v36, v42
	v_mul_f32_e32 v41, v41, v36
	v_fmamk_f32 v36, v186, 0x3c800000, v6
	v_min_f32_e32 v36, 0x40e00000, v36
	v_mul_f32_e32 v43, 0xc01d265f, v36
	v_exp_f32_e32 v43, v43
	v_fmamk_f32 v42, v154, 0x3c800000, v20
	v_med3_f32 v42, v42, s2, v250
	v_add_f32_e32 v43, 1.0, v43
	v_rcp_f32_e32 v43, v43
	s_nop 0
	v_mul_f32_e32 v36, v36, v43
	v_mul_f32_e32 v42, v42, v36
	v_fmamk_f32 v36, v187, 0x3c800000, v7
	v_min_f32_e32 v36, 0x40e00000, v36
	v_mul_f32_e32 v44, 0xc01d265f, v36
	v_exp_f32_e32 v44, v44
	v_fmamk_f32 v43, v155, 0x3c800000, v21
	v_med3_f32 v43, v43, s2, v250
	v_add_f32_e32 v44, 1.0, v44
	v_rcp_f32_e32 v44, v44
	s_nop 0
	v_mul_f32_e32 v36, v36, v44
	v_mul_f32_e32 v43, v43, v36
	v_mov_b32_e32 v36, v3
	v_cvt_pk_fp8_f32 v36, v31, v37
	v_mov_b32_e32 v37, v3
	v_cvt_pk_fp8_f32 v37, v40, v41
	v_fmamk_f32 v31, v180, 0x3c800000, v8
	v_min_f32_e32 v31, 0x40e00000, v31
	v_cvt_pk_fp8_f32 v36, v38, v39 op_sel:[0,0,1]
	v_cvt_pk_fp8_f32 v37, v42, v43 op_sel:[0,0,1]
	s_nop 0
	global_store_dwordx2 v[34:35], v[36:37], off sc1
	v_mul_f32_e32 v37, 0xc01d265f, v31
	v_exp_f32_e32 v37, v37
	v_fmamk_f32 v36, v148, 0x3c800000, v32
	v_med3_f32 v36, v36, s2, v250
	v_or_b32_e32 v34, 32, v30
	v_add_f32_e32 v37, 1.0, v37
	v_rcp_f32_e32 v37, v37
	v_ashrrev_i32_e32 v35, 31, v34
	v_lshlrev_b64 v[34:35], 10, v[34:35]
	v_lshl_add_u64 v[34:35], s[14:15], 0, v[34:35]
	v_mul_f32_e32 v31, v31, v37
	v_mul_f32_e32 v31, v36, v31
	v_fmamk_f32 v36, v181, 0x3c800000, v9
	v_min_f32_e32 v36, 0x40e00000, v36
	v_mul_f32_e32 v38, 0xc01d265f, v36
	v_exp_f32_e32 v38, v38
	v_fmamk_f32 v37, v149, 0x3c800000, v33
	v_med3_f32 v37, v37, s2, v250
	v_lshl_add_u64 v[34:35], v[34:35], 0, s[0:1]
	v_add_f32_e32 v38, 1.0, v38
	v_rcp_f32_e32 v38, v38
	v_lshl_add_u64 v[34:35], v[34:35], 0, s[24:25]
	v_lshl_add_u64 v[34:35], v[34:35], 0, v[28:29]
	v_or_b32_e32 v30, 48, v30
	v_mul_f32_e32 v36, v36, v38
	v_mul_f32_e32 v37, v37, v36
	v_fmamk_f32 v36, v182, 0x3c800000, v10
	v_min_f32_e32 v36, 0x40e00000, v36
	v_mul_f32_e32 v39, 0xc01d265f, v36
	v_exp_f32_e32 v39, v39
	v_fmamk_f32 v38, v150, 0x3c800000, v26
	v_med3_f32 v38, v38, s2, v250
	v_add_f32_e32 v39, 1.0, v39
	v_rcp_f32_e32 v39, v39
	s_nop 0
	v_mul_f32_e32 v36, v36, v39
	v_mul_f32_e32 v38, v38, v36
	v_fmamk_f32 v36, v183, 0x3c800000, v11
	v_min_f32_e32 v36, 0x40e00000, v36
	v_mul_f32_e32 v40, 0xc01d265f, v36
	v_exp_f32_e32 v40, v40
	v_fmamk_f32 v39, v151, 0x3c800000, v27
	v_med3_f32 v39, v39, s2, v250
	v_add_f32_e32 v40, 1.0, v40
	v_rcp_f32_e32 v40, v40
	s_nop 0
	v_mul_f32_e32 v36, v36, v40
	v_mul_f32_e32 v39, v39, v36
	v_fmamk_f32 v36, v176, 0x3c800000, v4
	v_min_f32_e32 v36, 0x40e00000, v36
	v_mul_f32_e32 v41, 0xc01d265f, v36
	v_exp_f32_e32 v41, v41
	v_fmamk_f32 v40, v144, 0x3c800000, v22
	v_med3_f32 v40, v40, s2, v250
	v_add_f32_e32 v41, 1.0, v41
	v_rcp_f32_e32 v41, v41
	s_nop 0
	v_mul_f32_e32 v36, v36, v41
	v_mul_f32_e32 v40, v40, v36
	v_fmamk_f32 v36, v177, 0x3c800000, v5
	v_min_f32_e32 v36, 0x40e00000, v36
	v_mul_f32_e32 v42, 0xc01d265f, v36
	v_exp_f32_e32 v42, v42
	v_fmamk_f32 v41, v145, 0x3c800000, v23
	v_med3_f32 v41, v41, s2, v250
	v_add_f32_e32 v42, 1.0, v42
	v_rcp_f32_e32 v42, v42
	s_nop 0
	v_mul_f32_e32 v36, v36, v42
	v_mul_f32_e32 v41, v41, v36
	v_fmamk_f32 v36, v178, 0x3c800000, v6
	v_min_f32_e32 v36, 0x40e00000, v36
	v_mul_f32_e32 v43, 0xc01d265f, v36
	v_exp_f32_e32 v43, v43
	v_fmamk_f32 v42, v146, 0x3c800000, v20
	v_med3_f32 v42, v42, s2, v250
	v_add_f32_e32 v43, 1.0, v43
	v_rcp_f32_e32 v43, v43
	s_nop 0
	v_mul_f32_e32 v36, v36, v43
	v_mul_f32_e32 v42, v42, v36
	v_fmamk_f32 v36, v179, 0x3c800000, v7
	v_min_f32_e32 v36, 0x40e00000, v36
	v_mul_f32_e32 v44, 0xc01d265f, v36
	v_exp_f32_e32 v44, v44
	v_fmamk_f32 v43, v147, 0x3c800000, v21
	v_med3_f32 v43, v43, s2, v250
	v_add_f32_e32 v44, 1.0, v44
	v_rcp_f32_e32 v44, v44
	s_nop 0
	v_mul_f32_e32 v36, v36, v44
	v_mul_f32_e32 v43, v43, v36
	v_mov_b32_e32 v36, v3
	v_cvt_pk_fp8_f32 v36, v31, v37
	v_mov_b32_e32 v37, v3
	v_cvt_pk_fp8_f32 v37, v40, v41
	v_ashrrev_i32_e32 v31, 31, v30
	v_cvt_pk_fp8_f32 v36, v38, v39 op_sel:[0,0,1]
	v_lshlrev_b64 v[30:31], 10, v[30:31]
	v_cvt_pk_fp8_f32 v37, v42, v43 op_sel:[0,0,1]
	v_lshl_add_u64 v[30:31], s[14:15], 0, v[30:31]
	global_store_dwordx2 v[34:35], v[36:37], off sc1
	v_fmamk_f32 v34, v172, 0x3c800000, v8
	v_min_f32_e32 v34, 0x40e00000, v34
	v_mul_f32_e32 v36, 0xc01d265f, v34
	v_exp_f32_e32 v36, v36
	v_fmamk_f32 v35, v140, 0x3c800000, v32
	v_med3_f32 v35, v35, s2, v250
	v_lshl_add_u64 v[30:31], v[30:31], 0, s[0:1]
	v_add_f32_e32 v36, 1.0, v36
	v_rcp_f32_e32 v36, v36
	v_lshl_add_u64 v[30:31], v[30:31], 0, s[24:25]
	v_lshl_add_u64 v[28:29], v[30:31], 0, v[28:29]
	v_mov_b32_e32 v30, v3
	v_mul_f32_e32 v34, v34, v36
	v_mul_f32_e32 v34, v35, v34
	v_fmamk_f32 v35, v173, 0x3c800000, v9
	v_min_f32_e32 v35, 0x40e00000, v35
	v_mul_f32_e32 v37, 0xc01d265f, v35
	v_exp_f32_e32 v37, v37
	v_fmamk_f32 v36, v141, 0x3c800000, v33
	v_med3_f32 v36, v36, s2, v250
	v_mov_b32_e32 v31, v3
	v_add_f32_e32 v37, 1.0, v37
	v_rcp_f32_e32 v37, v37
	s_mov_b64 s[0:1], 0x20000
	v_mul_f32_e32 v35, v35, v37
	v_mul_f32_e32 v35, v36, v35
	v_fmamk_f32 v36, v174, 0x3c800000, v10
	v_min_f32_e32 v36, 0x40e00000, v36
	v_mul_f32_e32 v38, 0xc01d265f, v36
	v_exp_f32_e32 v38, v38
	v_fmamk_f32 v37, v142, 0x3c800000, v26
	v_med3_f32 v37, v37, s2, v250
	v_cvt_pk_fp8_f32 v30, v34, v35
	v_add_f32_e32 v38, 1.0, v38
	v_rcp_f32_e32 v38, v38
	s_nop 0
	v_mul_f32_e32 v36, v36, v38
	v_mul_f32_e32 v36, v37, v36
	v_fmamk_f32 v37, v175, 0x3c800000, v11
	v_min_f32_e32 v37, 0x40e00000, v37
	v_mul_f32_e32 v39, 0xc01d265f, v37
	v_exp_f32_e32 v39, v39
	v_fmamk_f32 v38, v143, 0x3c800000, v27
	v_med3_f32 v38, v38, s2, v250
	v_add_f32_e32 v39, 1.0, v39
	v_rcp_f32_e32 v39, v39
	s_nop 0
	v_mul_f32_e32 v37, v37, v39
	v_mul_f32_e32 v37, v38, v37
	v_fmamk_f32 v38, v168, 0x3c800000, v4
	v_min_f32_e32 v38, 0x40e00000, v38
	v_mul_f32_e32 v40, 0xc01d265f, v38
	v_exp_f32_e32 v40, v40
	v_fmamk_f32 v39, v136, 0x3c800000, v22
	v_med3_f32 v39, v39, s2, v250
	v_cvt_pk_fp8_f32 v30, v36, v37 op_sel:[0,0,1]
	v_add_f32_e32 v40, 1.0, v40
	v_rcp_f32_e32 v40, v40
	s_nop 0
	v_mul_f32_e32 v38, v38, v40
	v_mul_f32_e32 v38, v39, v38
	v_fmamk_f32 v39, v169, 0x3c800000, v5
	v_min_f32_e32 v39, 0x40e00000, v39
	v_mul_f32_e32 v41, 0xc01d265f, v39
	v_exp_f32_e32 v41, v41
	v_fmamk_f32 v40, v137, 0x3c800000, v23
	v_med3_f32 v40, v40, s2, v250
	v_add_f32_e32 v41, 1.0, v41
	v_rcp_f32_e32 v41, v41
	s_nop 0
	v_mul_f32_e32 v39, v39, v41
	v_mul_f32_e32 v39, v40, v39
	v_fmamk_f32 v40, v170, 0x3c800000, v6
	v_min_f32_e32 v40, 0x40e00000, v40
	v_mul_f32_e32 v42, 0xc01d265f, v40
	v_exp_f32_e32 v42, v42
	v_fmamk_f32 v41, v138, 0x3c800000, v20
	v_med3_f32 v41, v41, s2, v250
	v_cvt_pk_fp8_f32 v31, v38, v39
	v_add_f32_e32 v42, 1.0, v42
	v_rcp_f32_e32 v42, v42
	s_nop 0
	v_mul_f32_e32 v40, v40, v42
	v_mul_f32_e32 v40, v41, v40
	v_fmamk_f32 v41, v171, 0x3c800000, v7
	v_min_f32_e32 v41, 0x40e00000, v41
	v_mul_f32_e32 v43, 0xc01d265f, v41
	v_exp_f32_e32 v43, v43
	v_fmamk_f32 v42, v139, 0x3c800000, v21
	v_med3_f32 v42, v42, s2, v250
	v_add_f32_e32 v43, 1.0, v43
	v_rcp_f32_e32 v43, v43
	s_nop 0
	v_mul_f32_e32 v41, v41, v43
	v_mul_f32_e32 v41, v42, v41
	v_cvt_pk_fp8_f32 v31, v40, v41 op_sel:[0,0,1]
	s_nop 0
	global_store_dwordx2 v[28:29], v[30:31], off sc1
	v_fmamk_f32 v28, v132, 0x3c800000, v8
	v_min_f32_e32 v28, 0x40e00000, v28
	v_mul_f32_e32 v30, 0xc01d265f, v28
	v_exp_f32_e32 v30, v30
	v_fmamk_f32 v29, v100, 0x3c800000, v32
	v_med3_f32 v29, v29, s2, v250
	v_add_f32_e32 v30, 1.0, v30
	v_rcp_f32_e32 v30, v30
	s_nop 0
	v_mul_f32_e32 v28, v28, v30
	v_mul_f32_e32 v31, v29, v28
	v_fmamk_f32 v28, v133, 0x3c800000, v9
	v_min_f32_e32 v28, 0x40e00000, v28
	v_mul_f32_e32 v30, 0xc01d265f, v28
	v_exp_f32_e32 v30, v30
	v_fmamk_f32 v29, v101, 0x3c800000, v33
	v_med3_f32 v29, v29, s2, v250
	v_add_f32_e32 v30, 1.0, v30
	v_rcp_f32_e32 v30, v30
	s_nop 0
	v_mul_f32_e32 v28, v28, v30
	v_mul_f32_e32 v34, v29, v28
	v_fmamk_f32 v28, v134, 0x3c800000, v10
	v_min_f32_e32 v28, 0x40e00000, v28
	v_mul_f32_e32 v30, 0xc01d265f, v28
	v_exp_f32_e32 v30, v30
	v_fmamk_f32 v29, v102, 0x3c800000, v26
	v_med3_f32 v29, v29, s2, v250
	v_add_f32_e32 v30, 1.0, v30
	v_rcp_f32_e32 v30, v30
	s_nop 0
	v_mul_f32_e32 v28, v28, v30
	v_mul_f32_e32 v35, v29, v28
	v_fmamk_f32 v28, v135, 0x3c800000, v11
	v_min_f32_e32 v28, 0x40e00000, v28
	v_mul_f32_e32 v30, 0xc01d265f, v28
	v_exp_f32_e32 v30, v30
	v_fmamk_f32 v29, v103, 0x3c800000, v27
	v_med3_f32 v29, v29, s2, v250
	v_add_f32_e32 v30, 1.0, v30
	v_rcp_f32_e32 v30, v30
	s_nop 0
	v_mul_f32_e32 v28, v28, v30
	v_mul_f32_e32 v36, v29, v28
	v_fmamk_f32 v28, v128, 0x3c800000, v4
	v_min_f32_e32 v28, 0x40e00000, v28
	v_mul_f32_e32 v30, 0xc01d265f, v28
	v_exp_f32_e32 v30, v30
	v_fmamk_f32 v29, v96, 0x3c800000, v22
	v_med3_f32 v29, v29, s2, v250
	v_add_f32_e32 v30, 1.0, v30
	v_rcp_f32_e32 v30, v30
	s_nop 0
	v_mul_f32_e32 v28, v28, v30
	v_mul_f32_e32 v37, v29, v28
	v_fmamk_f32 v28, v129, 0x3c800000, v5
	v_min_f32_e32 v28, 0x40e00000, v28
	v_mul_f32_e32 v30, 0xc01d265f, v28
	v_exp_f32_e32 v30, v30
	v_fmamk_f32 v29, v97, 0x3c800000, v23
	v_med3_f32 v29, v29, s2, v250
	v_add_f32_e32 v30, 1.0, v30
	v_rcp_f32_e32 v30, v30
	s_nop 0
	v_mul_f32_e32 v28, v28, v30
	v_mul_f32_e32 v38, v29, v28
	v_fmamk_f32 v28, v130, 0x3c800000, v6
	v_min_f32_e32 v28, 0x40e00000, v28
	v_mul_f32_e32 v30, 0xc01d265f, v28
	v_exp_f32_e32 v30, v30
	v_fmamk_f32 v29, v98, 0x3c800000, v20
	v_med3_f32 v29, v29, s2, v250
	v_add_f32_e32 v30, 1.0, v30
	v_rcp_f32_e32 v30, v30
	s_nop 0
	v_mul_f32_e32 v28, v28, v30
	v_mul_f32_e32 v39, v29, v28
	v_fmamk_f32 v28, v131, 0x3c800000, v7
	v_min_f32_e32 v28, 0x40e00000, v28
	v_mul_f32_e32 v30, 0xc01d265f, v28
	v_exp_f32_e32 v30, v30
	v_fmamk_f32 v29, v99, 0x3c800000, v21
	v_med3_f32 v29, v29, s2, v250
	v_add_f32_e32 v30, 1.0, v30
	v_rcp_f32_e32 v30, v30
	s_nop 0
	v_mul_f32_e32 v28, v28, v30
	v_mov_b32_e32 v30, v3
	v_cvt_pk_fp8_f32 v30, v31, v34
	v_mov_b32_e32 v31, v3
	v_cvt_pk_fp8_f32 v31, v37, v38
	v_mul_f32_e32 v40, v29, v28
	v_lshl_add_u64 v[28:29], v[24:25], 0, s[0:1]
	v_cvt_pk_fp8_f32 v30, v35, v36 op_sel:[0,0,1]
	v_cvt_pk_fp8_f32 v31, v39, v40 op_sel:[0,0,1]
	s_mov_b64 s[0:1], 0x24000
	global_store_dwordx2 v[28:29], v[30:31], off sc1
	v_fmamk_f32 v28, v124, 0x3c800000, v8
	v_min_f32_e32 v28, 0x40e00000, v28
	v_mul_f32_e32 v30, 0xc01d265f, v28
	v_exp_f32_e32 v30, v30
	v_fmamk_f32 v29, v92, 0x3c800000, v32
	v_med3_f32 v29, v29, s2, v250
	v_add_f32_e32 v30, 1.0, v30
	v_rcp_f32_e32 v30, v30
	s_nop 0
	v_mul_f32_e32 v28, v28, v30
	v_mul_f32_e32 v31, v29, v28
	v_fmamk_f32 v28, v125, 0x3c800000, v9
	v_min_f32_e32 v28, 0x40e00000, v28
	v_mul_f32_e32 v30, 0xc01d265f, v28
	v_exp_f32_e32 v30, v30
	v_fmamk_f32 v29, v93, 0x3c800000, v33
	v_med3_f32 v29, v29, s2, v250
	v_add_f32_e32 v30, 1.0, v30
	v_rcp_f32_e32 v30, v30
	s_nop 0
	v_mul_f32_e32 v28, v28, v30
	v_mul_f32_e32 v34, v29, v28
	v_fmamk_f32 v28, v126, 0x3c800000, v10
	v_min_f32_e32 v28, 0x40e00000, v28
	v_mul_f32_e32 v30, 0xc01d265f, v28
	v_exp_f32_e32 v30, v30
	v_fmamk_f32 v29, v94, 0x3c800000, v26
	v_med3_f32 v29, v29, s2, v250
	v_add_f32_e32 v30, 1.0, v30
	v_rcp_f32_e32 v30, v30
	s_nop 0
	v_mul_f32_e32 v28, v28, v30
	v_mul_f32_e32 v35, v29, v28
	v_fmamk_f32 v28, v127, 0x3c800000, v11
	v_min_f32_e32 v28, 0x40e00000, v28
	v_mul_f32_e32 v30, 0xc01d265f, v28
	v_exp_f32_e32 v30, v30
	v_fmamk_f32 v29, v95, 0x3c800000, v27
	v_med3_f32 v29, v29, s2, v250
	v_add_f32_e32 v30, 1.0, v30
	v_rcp_f32_e32 v30, v30
	s_nop 0
	v_mul_f32_e32 v28, v28, v30
	v_mul_f32_e32 v36, v29, v28
	v_fmamk_f32 v28, v120, 0x3c800000, v4
	v_min_f32_e32 v28, 0x40e00000, v28
	v_mul_f32_e32 v30, 0xc01d265f, v28
	v_exp_f32_e32 v30, v30
	v_fmamk_f32 v29, v88, 0x3c800000, v22
	v_med3_f32 v29, v29, s2, v250
	v_add_f32_e32 v30, 1.0, v30
	v_rcp_f32_e32 v30, v30
	s_nop 0
	v_mul_f32_e32 v28, v28, v30
	v_mul_f32_e32 v37, v29, v28
	v_fmamk_f32 v28, v121, 0x3c800000, v5
	v_min_f32_e32 v28, 0x40e00000, v28
	v_mul_f32_e32 v30, 0xc01d265f, v28
	v_exp_f32_e32 v30, v30
	v_fmamk_f32 v29, v89, 0x3c800000, v23
	v_med3_f32 v29, v29, s2, v250
	v_add_f32_e32 v30, 1.0, v30
	v_rcp_f32_e32 v30, v30
	s_nop 0
	v_mul_f32_e32 v28, v28, v30
	v_mul_f32_e32 v38, v29, v28
	v_fmamk_f32 v28, v122, 0x3c800000, v6
	v_min_f32_e32 v28, 0x40e00000, v28
	v_mul_f32_e32 v30, 0xc01d265f, v28
	v_exp_f32_e32 v30, v30
	v_fmamk_f32 v29, v90, 0x3c800000, v20
	v_med3_f32 v29, v29, s2, v250
	v_add_f32_e32 v30, 1.0, v30
	v_rcp_f32_e32 v30, v30
	s_nop 0
	v_mul_f32_e32 v28, v28, v30
	v_mul_f32_e32 v39, v29, v28
	v_fmamk_f32 v28, v123, 0x3c800000, v7
	v_min_f32_e32 v28, 0x40e00000, v28
	v_mul_f32_e32 v30, 0xc01d265f, v28
	v_exp_f32_e32 v30, v30
	v_fmamk_f32 v29, v91, 0x3c800000, v21
	v_med3_f32 v29, v29, s2, v250
	v_add_f32_e32 v30, 1.0, v30
	v_rcp_f32_e32 v30, v30
	s_nop 0
	v_mul_f32_e32 v28, v28, v30
	v_mov_b32_e32 v30, v3
	v_cvt_pk_fp8_f32 v30, v31, v34
	v_mov_b32_e32 v31, v3
	v_cvt_pk_fp8_f32 v31, v37, v38
	v_mul_f32_e32 v40, v29, v28
	v_lshl_add_u64 v[28:29], v[24:25], 0, s[0:1]
	v_cvt_pk_fp8_f32 v30, v35, v36 op_sel:[0,0,1]
	v_cvt_pk_fp8_f32 v31, v39, v40 op_sel:[0,0,1]
	s_mov_b64 s[0:1], 0x28000
	global_store_dwordx2 v[28:29], v[30:31], off sc1
	v_fmamk_f32 v28, v116, 0x3c800000, v8
	v_min_f32_e32 v28, 0x40e00000, v28
	v_mul_f32_e32 v30, 0xc01d265f, v28
	v_exp_f32_e32 v30, v30
	v_fmamk_f32 v29, v84, 0x3c800000, v32
	v_med3_f32 v29, v29, s2, v250
	v_fmamk_f32 v8, v108, 0x3c800000, v8
	v_add_f32_e32 v30, 1.0, v30
	v_rcp_f32_e32 v30, v30
	v_min_f32_e32 v8, 0x40e00000, v8
	v_mul_f32_e32 v28, v28, v30
	v_mul_f32_e32 v31, v29, v28
	v_fmamk_f32 v28, v117, 0x3c800000, v9
	v_min_f32_e32 v28, 0x40e00000, v28
	v_mul_f32_e32 v30, 0xc01d265f, v28
	v_exp_f32_e32 v30, v30
	v_fmamk_f32 v29, v85, 0x3c800000, v33
	v_med3_f32 v29, v29, s2, v250
	v_fmamk_f32 v9, v109, 0x3c800000, v9
	v_add_f32_e32 v30, 1.0, v30
	v_rcp_f32_e32 v30, v30
	v_min_f32_e32 v9, 0x40e00000, v9
	v_fmac_f32_e32 v33, 0x3c800000, v77
	v_mul_f32_e32 v28, v28, v30
	v_mul_f32_e32 v34, v29, v28
	v_fmamk_f32 v28, v118, 0x3c800000, v10
	v_min_f32_e32 v28, 0x40e00000, v28
	v_mul_f32_e32 v30, 0xc01d265f, v28
	v_exp_f32_e32 v30, v30
	v_fmamk_f32 v29, v86, 0x3c800000, v26
	v_med3_f32 v29, v29, s2, v250
	v_fmamk_f32 v10, v110, 0x3c800000, v10
	v_add_f32_e32 v30, 1.0, v30
	v_rcp_f32_e32 v30, v30
	v_min_f32_e32 v10, 0x40e00000, v10
	v_fmamk_f32 v26, v78, 0x3c800000, v26
	v_med3_f32 v26, v26, s2, v250
	v_mul_f32_e32 v28, v28, v30
	v_mul_f32_e32 v35, v29, v28
	v_fmamk_f32 v28, v119, 0x3c800000, v11
	v_min_f32_e32 v28, 0x40e00000, v28
	v_mul_f32_e32 v30, 0xc01d265f, v28
	v_exp_f32_e32 v30, v30
	v_fmamk_f32 v29, v87, 0x3c800000, v27
	v_med3_f32 v29, v29, s2, v250
	v_fmac_f32_e32 v11, 0x3c800000, v111
	v_add_f32_e32 v30, 1.0, v30
	v_rcp_f32_e32 v30, v30
	v_min_f32_e32 v11, 0x40e00000, v11
	v_fmac_f32_e32 v27, 0x3c800000, v79
	v_mul_f32_e32 v28, v28, v30
	v_mul_f32_e32 v36, v29, v28
	v_fmamk_f32 v28, v112, 0x3c800000, v4
	v_min_f32_e32 v28, 0x40e00000, v28
	v_mul_f32_e32 v30, 0xc01d265f, v28
	v_exp_f32_e32 v30, v30
	v_fmamk_f32 v29, v80, 0x3c800000, v22
	v_med3_f32 v29, v29, s2, v250
	v_fmamk_f32 v4, v104, 0x3c800000, v4
	v_add_f32_e32 v30, 1.0, v30
	v_rcp_f32_e32 v30, v30
	v_min_f32_e32 v4, 0x40e00000, v4
	v_fmamk_f32 v22, v12, 0x3c800000, v22
	v_med3_f32 v22, v22, s2, v250
	v_mul_f32_e32 v28, v28, v30
	v_mul_f32_e32 v37, v29, v28
	v_fmamk_f32 v28, v113, 0x3c800000, v5
	v_min_f32_e32 v28, 0x40e00000, v28
	v_mul_f32_e32 v30, 0xc01d265f, v28
	v_exp_f32_e32 v30, v30
	v_fmamk_f32 v29, v81, 0x3c800000, v23
	v_med3_f32 v29, v29, s2, v250
	v_fmac_f32_e32 v23, 0x3c800000, v13
	v_add_f32_e32 v30, 1.0, v30
	v_rcp_f32_e32 v30, v30
	s_nop 0
	v_mul_f32_e32 v28, v28, v30
	v_mul_f32_e32 v38, v29, v28
	v_fmamk_f32 v28, v114, 0x3c800000, v6
	v_min_f32_e32 v28, 0x40e00000, v28
	v_mul_f32_e32 v30, 0xc01d265f, v28
	v_exp_f32_e32 v30, v30
	v_fmamk_f32 v29, v82, 0x3c800000, v20
	v_med3_f32 v29, v29, s2, v250
	v_add_f32_e32 v30, 1.0, v30
	v_rcp_f32_e32 v30, v30
	s_nop 0
	v_mul_f32_e32 v28, v28, v30
	v_mul_f32_e32 v39, v29, v28
	v_fmamk_f32 v28, v115, 0x3c800000, v7
	v_min_f32_e32 v28, 0x40e00000, v28
	v_mul_f32_e32 v30, 0xc01d265f, v28
	v_exp_f32_e32 v30, v30
	v_fmamk_f32 v29, v83, 0x3c800000, v21
	v_med3_f32 v29, v29, s2, v250
	v_fmac_f32_e32 v7, 0x3c800000, v107
	v_add_f32_e32 v30, 1.0, v30
	v_rcp_f32_e32 v30, v30
	v_fmac_f32_e32 v21, 0x3c800000, v15
	v_mul_f32_e32 v28, v28, v30
	v_mov_b32_e32 v30, v3
	v_cvt_pk_fp8_f32 v30, v31, v34
	v_mov_b32_e32 v31, v3
	v_cvt_pk_fp8_f32 v31, v37, v38
	v_mul_f32_e32 v40, v29, v28
	v_lshl_add_u64 v[28:29], v[24:25], 0, s[0:1]
	v_cvt_pk_fp8_f32 v30, v35, v36 op_sel:[0,0,1]
	v_cvt_pk_fp8_f32 v31, v39, v40 op_sel:[0,0,1]
	s_mov_b64 s[0:1], 0x2c000
	global_store_dwordx2 v[28:29], v[30:31], off sc1
	v_mul_f32_e32 v29, 0xc01d265f, v8
	v_exp_f32_e32 v29, v29
	v_fmamk_f32 v28, v76, 0x3c800000, v32
	v_med3_f32 v28, v28, s2, v250
	v_add_f32_e32 v29, 1.0, v29
	v_rcp_f32_e32 v29, v29
	s_nop 0
	v_mul_f32_e32 v8, v8, v29
	v_mul_f32_e32 v29, 0xc01d265f, v9
	v_exp_f32_e32 v29, v29
	v_mul_f32_e32 v8, v28, v8
	v_med3_f32 v28, v33, s2, v250
	v_add_f32_e32 v29, 1.0, v29
	v_rcp_f32_e32 v29, v29
	s_nop 0
	v_mul_f32_e32 v9, v9, v29
	v_mul_f32_e32 v9, v28, v9
	v_mul_f32_e32 v28, 0xc01d265f, v10
	v_exp_f32_e32 v28, v28
	s_nop 0
	v_add_f32_e32 v28, 1.0, v28
	v_rcp_f32_e32 v28, v28
	s_nop 0
	v_mul_f32_e32 v10, v10, v28
	v_mul_f32_e32 v10, v26, v10
	v_med3_f32 v26, v27, s2, v250
	v_mul_f32_e32 v27, 0xc01d265f, v11
	v_exp_f32_e32 v27, v27
	s_nop 0
	v_add_f32_e32 v27, 1.0, v27
	v_rcp_f32_e32 v27, v27
	s_nop 0
	v_mul_f32_e32 v11, v11, v27
	v_mul_f32_e32 v11, v26, v11
	v_mul_f32_e32 v26, 0xc01d265f, v4
	v_exp_f32_e32 v26, v26
	s_nop 0
	v_add_f32_e32 v26, 1.0, v26
	v_rcp_f32_e32 v26, v26
	s_nop 0
	v_mul_f32_e32 v4, v4, v26
	v_mul_f32_e32 v22, v22, v4
	v_fmamk_f32 v4, v105, 0x3c800000, v5
	v_min_f32_e32 v4, 0x40e00000, v4
	v_med3_f32 v5, v23, s2, v250
	v_mul_f32_e32 v23, 0xc01d265f, v4
	v_exp_f32_e32 v23, v23
	s_nop 0
	v_add_f32_e32 v23, 1.0, v23
	v_rcp_f32_e32 v23, v23
	s_nop 0
	v_mul_f32_e32 v4, v4, v23
	v_mul_f32_e32 v23, v5, v4
	v_fmamk_f32 v4, v106, 0x3c800000, v6
	v_min_f32_e32 v4, 0x40e00000, v4
	v_mul_f32_e32 v6, 0xc01d265f, v4
	v_exp_f32_e32 v6, v6
	v_fmamk_f32 v5, v14, 0x3c800000, v20
	v_med3_f32 v5, v5, s2, v250
	v_add_f32_e32 v6, 1.0, v6
	v_rcp_f32_e32 v6, v6
	s_nop 0
	v_mul_f32_e32 v4, v4, v6
	v_mul_f32_e32 v20, v5, v4
	v_min_f32_e32 v4, 0x40e00000, v7
	v_mul_f32_e32 v6, 0xc01d265f, v4
	v_exp_f32_e32 v6, v6
	v_mov_b32_e32 v7, v3
	v_cvt_pk_fp8_f32 v7, v22, v23
	v_med3_f32 v5, v21, s2, v250
	v_add_f32_e32 v6, 1.0, v6
	v_rcp_f32_e32 v6, v6
	s_nop 0
	v_mul_f32_e32 v4, v4, v6
	v_mov_b32_e32 v6, v3
	v_cvt_pk_fp8_f32 v6, v8, v9
	v_mul_f32_e32 v21, v5, v4
	v_lshl_add_u64 v[4:5], v[24:25], 0, s[0:1]
	v_cvt_pk_fp8_f32 v7, v20, v21 op_sel:[0,0,1]
	v_cvt_pk_fp8_f32 v6, v10, v11 op_sel:[0,0,1]
	s_nop 0
	global_store_dwordx2 v[4:5], v[6:7], off sc1
